# threshold-lane search: 16 independent readlanes + scalar scan instead of the VALU<->SALU loop (on top of the union v44)
# speedup vs baseline: 1.0108x; 1.0044x over previous
.LBB0_720:
	s_or_b64 exec, exec, s[0:1]
	v_readfirstlane_b32 s8, v2
	s_cmp_gt_u32 s8, 31
	s_mov_b64 s[0:1], -1
	s_cbranch_scc1 .LBB0_715
	s_sub_i32 s0, 31, s8
	s_or_b32 s97, s0, s6
	s_lshl_b32 s1, s0, 14
	v_readlane_b32 s8, v254, 51
	s_add_u32 s8, s8, s1
	v_readlane_b32 s1, v254, 52
	v_mov_b32_e32 v10, v200
	s_addc_u32 s9, s1, 0
	s_mov_b32 s1, 0
	v_ashrrev_i32_e32 v11, 31, v10
	s_waitcnt lgkmcnt(1)
	v_lshl_add_u64 v[2:3], v[10:11], 2, s[8:9]
	global_load_dword v8, v[2:3], off
	global_load_dword v9, v[2:3], off offset:256
	global_load_dword v11, v[2:3], off offset:512
	global_load_dword v12, v[2:3], off offset:768
	global_load_dword v13, v[2:3], off offset:1024
	global_load_dword v14, v[2:3], off offset:1280
	global_load_dword v15, v[2:3], off offset:1536
	global_load_dword v16, v[2:3], off offset:1792
	global_load_dword v17, v[2:3], off offset:2048
	global_load_dword v18, v[2:3], off offset:2304
	global_load_dword v19, v[2:3], off offset:2560
	global_load_dword v20, v[2:3], off offset:2816
	global_load_dword v21, v[2:3], off offset:3072
	global_load_dword v22, v[2:3], off offset:3328
	global_load_dword v23, v[2:3], off offset:3584
	global_load_dword v24, v[2:3], off offset:3840
	s_movk_i32 s8, 0x1000
	s_waitcnt lgkmcnt(0)
	v_add_co_u32_e32 v4, vcc, s8, v2
	s_movk_i32 s8, 0x2000
	s_nop 0
	v_addc_co_u32_e32 v5, vcc, 0, v3, vcc
	v_add_co_u32_e32 v6, vcc, s8, v2
	s_movk_i32 s8, 0x3000
	s_nop 0
	v_addc_co_u32_e32 v7, vcc, 0, v3, vcc
	v_cmp_gt_i32_e32 vcc, s52, v10
	global_load_dword v25, v[6:7], off offset:-4096
	global_load_dword v26, v[4:5], off offset:256
	global_load_dword v27, v[4:5], off offset:512
	global_load_dword v28, v[4:5], off offset:768
	global_load_dword v29, v[4:5], off offset:1024
	global_load_dword v30, v[4:5], off offset:1280
	global_load_dword v31, v[4:5], off offset:1536
	global_load_dword v32, v[4:5], off offset:1792
	global_load_dword v33, v[4:5], off offset:2048
	global_load_dword v34, v[4:5], off offset:2304
	global_load_dword v35, v[4:5], off offset:2560
	global_load_dword v36, v[4:5], off offset:2816
	global_load_dword v37, v[4:5], off offset:3072
	global_load_dword v38, v[4:5], off offset:3328
	global_load_dword v39, v[4:5], off offset:3584
	s_nop 0
	global_load_dword v4, v[4:5], off offset:3840
	s_nop 0
	global_load_dword v5, v[6:7], off
	global_load_dword v40, v[6:7], off offset:256
	global_load_dword v41, v[6:7], off offset:512
	global_load_dword v42, v[6:7], off offset:768
	global_load_dword v78, v[6:7], off offset:1024
	global_load_dword v79, v[6:7], off offset:1280
	global_load_dword v80, v[6:7], off offset:1536
	global_load_dword v81, v[6:7], off offset:1792
	s_cmpk_lt_i32 s97, 0x100
	s_waitcnt vmcnt(39)
	v_cndmask_b32_e32 v77, 0, v8, vcc
	v_cmp_gt_i32_e32 vcc, s26, v10
	global_load_dword v8, v[6:7], off offset:2048
	s_waitcnt vmcnt(39)
	v_cndmask_b32_e32 v76, 0, v9, vcc
	v_cmp_gt_i32_e32 vcc, s27, v10
	s_waitcnt vmcnt(38)
	s_nop 0
	v_cndmask_b32_e32 v75, 0, v11, vcc
	v_cmp_gt_i32_e32 vcc, s28, v10
	global_load_dword v9, v[6:7], off offset:2304
	global_load_dword v11, v[6:7], off offset:2560
	s_waitcnt vmcnt(39)
	v_cndmask_b32_e32 v74, 0, v12, vcc
	v_cmp_gt_i32_e32 vcc, s29, v10
	s_waitcnt vmcnt(38)
	s_nop 0
	v_cndmask_b32_e32 v73, 0, v13, vcc
	v_cmp_gt_i32_e32 vcc, s30, v10
	s_waitcnt vmcnt(37)
	s_nop 0
	v_cndmask_b32_e32 v72, 0, v14, vcc
	v_cmp_gt_i32_e32 vcc, s31, v10
	s_waitcnt vmcnt(36)
	s_nop 0
	v_cndmask_b32_e32 v71, 0, v15, vcc
	v_cmp_gt_i32_e32 vcc, s34, v10
	global_load_dword v12, v[6:7], off offset:2816
	global_load_dword v13, v[6:7], off offset:3072
	global_load_dword v14, v[6:7], off offset:3328
	global_load_dword v15, v[6:7], off offset:3584
	s_nop 0
	global_load_dword v6, v[6:7], off offset:3840
	s_waitcnt vmcnt(40)
	v_cndmask_b32_e32 v70, 0, v16, vcc
	v_cmp_gt_i32_e32 vcc, s35, v10
	s_waitcnt vmcnt(39)
	s_nop 0
	v_cndmask_b32_e32 v69, 0, v17, vcc
	v_cmp_gt_i32_e32 vcc, s36, v10
	s_waitcnt vmcnt(38)
	s_nop 0
	v_cndmask_b32_e32 v68, 0, v18, vcc
	v_cmp_gt_i32_e32 vcc, s7, v10
	s_waitcnt vmcnt(37)
	s_nop 0
	v_cndmask_b32_e32 v67, 0, v19, vcc
	v_cmp_gt_i32_e32 vcc, s37, v10
	s_waitcnt vmcnt(36)
	s_nop 0
	v_cndmask_b32_e32 v66, 0, v20, vcc
	v_cmp_gt_i32_e32 vcc, s2, v10
	s_waitcnt vmcnt(35)
	s_nop 0
	v_cndmask_b32_e32 v65, 0, v21, vcc
	v_cmp_gt_i32_e32 vcc, s38, v10
	s_waitcnt vmcnt(34)
	s_nop 0
	v_cndmask_b32_e32 v64, 0, v22, vcc
	v_cmp_gt_i32_e32 vcc, s39, v10
	s_waitcnt vmcnt(33)
	s_nop 0
	v_cndmask_b32_e32 v63, 0, v23, vcc
	v_cmp_gt_i32_e32 vcc, s40, v10
	s_waitcnt vmcnt(32)
	s_nop 0
	v_cndmask_b32_e32 v62, 0, v24, vcc
	v_add_co_u32_e32 v2, vcc, s8, v2
	v_readlane_b32 s8, v255, 16
	s_nop 0
	v_addc_co_u32_e32 v3, vcc, 0, v3, vcc
	global_load_dword v7, v[2:3], off
	global_load_dword v16, v[2:3], off offset:256
	global_load_dword v17, v[2:3], off offset:512
	global_load_dword v18, v[2:3], off offset:768
	global_load_dword v19, v[2:3], off offset:1024
	global_load_dword v20, v[2:3], off offset:1280
	global_load_dword v21, v[2:3], off offset:1536
	global_load_dword v22, v[2:3], off offset:1792
	global_load_dword v82, v[2:3], off offset:2304
	global_load_dword v83, v[2:3], off offset:2560
	global_load_dword v84, v[2:3], off offset:2816
	global_load_dword v85, v[2:3], off offset:3072
	global_load_dword v86, v[2:3], off offset:3328
	global_load_dword v87, v[2:3], off offset:3584
	global_load_dword v88, v[2:3], off offset:3840
	v_cmp_gt_i32_e32 vcc, s41, v10
	global_load_dword v2, v[2:3], off offset:2048
	s_waitcnt vmcnt(47)
	v_cndmask_b32_e32 v61, 0, v25, vcc
	v_cmp_gt_i32_e32 vcc, s42, v10
	s_waitcnt vmcnt(46)
	s_nop 0
	v_cndmask_b32_e32 v60, 0, v26, vcc
	v_cmp_gt_i32_e32 vcc, s43, v10
	s_waitcnt vmcnt(45)
	s_nop 0
	v_cndmask_b32_e32 v59, 0, v27, vcc
	v_cmp_gt_i32_e32 vcc, s33, v10
	s_waitcnt vmcnt(44)
	s_nop 0
	v_cndmask_b32_e32 v58, 0, v28, vcc
	v_cmp_gt_i32_e32 vcc, s44, v10
	s_waitcnt vmcnt(43)
	s_nop 0
	v_cndmask_b32_e32 v57, 0, v29, vcc
	v_cmp_gt_i32_e32 vcc, s45, v10
	s_waitcnt vmcnt(42)
	s_nop 0
	v_cndmask_b32_e32 v56, 0, v30, vcc
	v_cmp_gt_i32_e32 vcc, s51, v10
	s_waitcnt vmcnt(41)
	s_nop 0
	v_cndmask_b32_e32 v55, 0, v31, vcc
	v_cmp_gt_i32_e32 vcc, s50, v10
	s_waitcnt vmcnt(40)
	s_nop 0
	v_cndmask_b32_e32 v54, 0, v32, vcc
	v_cmp_gt_i32_e32 vcc, s56, v10
	s_waitcnt vmcnt(39)
	s_nop 0
	v_cndmask_b32_e32 v53, 0, v33, vcc
	v_cmp_gt_i32_e32 vcc, s55, v10
	s_waitcnt vmcnt(38)
	s_nop 0
	v_cndmask_b32_e32 v52, 0, v34, vcc
	v_cmp_gt_i32_e32 vcc, s58, v10
	s_waitcnt vmcnt(37)
	s_nop 0
	v_cndmask_b32_e32 v51, 0, v35, vcc
	v_cmp_gt_i32_e32 vcc, s57, v10
	s_waitcnt vmcnt(36)
	s_nop 0
	v_cndmask_b32_e32 v50, 0, v36, vcc
	v_cmp_gt_i32_e32 vcc, s63, v10
	s_waitcnt vmcnt(35)
	s_nop 0
	v_cndmask_b32_e32 v49, 0, v37, vcc
	v_cmp_gt_i32_e32 vcc, s59, v10
	s_waitcnt vmcnt(34)
	s_nop 0
	v_cndmask_b32_e32 v48, 0, v38, vcc
	v_cmp_gt_i32_e32 vcc, s62, v10
	s_waitcnt vmcnt(33)
	s_nop 0
	v_cndmask_b32_e32 v47, 0, v39, vcc
	v_cmp_gt_i32_e32 vcc, s65, v10
	s_waitcnt vmcnt(32)
	s_nop 0
	v_cndmask_b32_e32 v46, 0, v4, vcc
	v_cmp_gt_i32_e32 vcc, s64, v10
	s_waitcnt vmcnt(31)
	s_nop 0
	v_cndmask_b32_e32 v45, 0, v5, vcc
	v_cmp_gt_i32_e32 vcc, s67, v10
	s_waitcnt vmcnt(30)
	s_nop 0
	v_cndmask_b32_e32 v44, 0, v40, vcc
	v_cmp_gt_i32_e32 vcc, s66, v10
	s_waitcnt vmcnt(29)
	s_nop 0
	v_cndmask_b32_e32 v43, 0, v41, vcc
	v_cmp_gt_i32_e32 vcc, s68, v10
	s_waitcnt vmcnt(28)
	s_nop 0
	v_cndmask_b32_e32 v42, 0, v42, vcc
	v_cmp_gt_i32_e32 vcc, s69, v10
	s_waitcnt vmcnt(27)
	s_nop 0
	v_cndmask_b32_e32 v41, 0, v78, vcc
	v_cmp_gt_i32_e32 vcc, s70, v10
	s_waitcnt vmcnt(26)
	s_nop 0
	v_cndmask_b32_e32 v40, 0, v79, vcc
	v_cmp_gt_i32_e32 vcc, s72, v10
	s_waitcnt vmcnt(25)
	s_nop 0
	v_cndmask_b32_e32 v39, 0, v80, vcc
	v_cmp_gt_i32_e32 vcc, s71, v10
	s_waitcnt vmcnt(24)
	s_nop 0
	v_cndmask_b32_e32 v38, 0, v81, vcc
	v_cmp_gt_i32_e32 vcc, s73, v10
	s_waitcnt vmcnt(23)
	s_nop 0
	v_cndmask_b32_e32 v37, 0, v8, vcc
	v_cmp_gt_i32_e32 vcc, s74, v10
	s_waitcnt vmcnt(22)
	s_nop 0
	v_cndmask_b32_e32 v36, 0, v9, vcc
	v_cmp_gt_i32_e32 vcc, s75, v10
	s_waitcnt vmcnt(21)
	s_nop 0
	v_cndmask_b32_e32 v35, 0, v11, vcc
	v_cmp_gt_i32_e32 vcc, s76, v10
	v_lshlrev_b32_e32 v11, 1, v10
	s_waitcnt vmcnt(20)
	v_cndmask_b32_e32 v34, 0, v12, vcc
	v_cmp_gt_i32_e32 vcc, s77, v10
	s_waitcnt vmcnt(19)
	s_nop 0
	v_cndmask_b32_e32 v33, 0, v13, vcc
	v_cmp_gt_i32_e32 vcc, s78, v10
	s_waitcnt vmcnt(18)
	s_nop 0
	v_cndmask_b32_e32 v32, 0, v14, vcc
	v_cmp_gt_i32_e32 vcc, s79, v10
	s_waitcnt vmcnt(17)
	s_nop 0
	v_cndmask_b32_e32 v31, 0, v15, vcc
	v_cmp_gt_i32_e32 vcc, s96, v10
	s_waitcnt vmcnt(16)
	s_nop 0
	v_cndmask_b32_e32 v30, 0, v6, vcc
	v_cmp_gt_i32_e32 vcc, s82, v10
	s_waitcnt vmcnt(15)
	s_nop 0
	v_cndmask_b32_e32 v29, 0, v7, vcc
	v_cmp_gt_i32_e32 vcc, s83, v10
	s_waitcnt vmcnt(14)
	s_nop 0
	v_cndmask_b32_e32 v28, 0, v16, vcc
	v_cmp_gt_i32_e32 vcc, s84, v10
	s_waitcnt vmcnt(13)
	s_nop 0
	v_cndmask_b32_e32 v27, 0, v17, vcc
	v_cmp_gt_i32_e32 vcc, s85, v10
	s_waitcnt vmcnt(12)
	s_nop 0
	v_cndmask_b32_e32 v26, 0, v18, vcc
	v_cmp_gt_i32_e32 vcc, s86, v10
	s_waitcnt vmcnt(11)
	s_nop 0
	v_cndmask_b32_e32 v25, 0, v19, vcc
	v_cmp_gt_i32_e32 vcc, s87, v10
	s_waitcnt vmcnt(10)
	s_nop 0
	v_cndmask_b32_e32 v24, 0, v20, vcc
	v_cmp_gt_i32_e32 vcc, s88, v10
	s_waitcnt vmcnt(9)
	s_nop 0
	v_cndmask_b32_e32 v23, 0, v21, vcc
	v_cmp_gt_i32_e32 vcc, s89, v10
	s_waitcnt vmcnt(8)
	s_nop 0
	v_cndmask_b32_e32 v22, 0, v22, vcc
	v_cmp_gt_i32_e32 vcc, s90, v10
	s_waitcnt vmcnt(0)
	s_nop 0
	v_cndmask_b32_e32 v21, 0, v2, vcc
	v_cmp_gt_i32_e32 vcc, s91, v10
	v_lshlrev_b64 v[2:3], v10, -1
	v_not_b32_e32 v12, v3
	v_cndmask_b32_e32 v20, 0, v82, vcc
	v_cmp_gt_i32_e32 vcc, s92, v10
	v_not_b32_e32 v13, v2
	s_nop 0
	v_cndmask_b32_e32 v19, 0, v83, vcc
	v_cmp_gt_i32_e32 vcc, s94, v10
	s_nop 1
	v_cndmask_b32_e32 v18, 0, v84, vcc
	v_cmp_gt_i32_e32 vcc, s8, v10
	v_readlane_b32 s8, v255, 17
	s_nop 0
	v_cndmask_b32_e32 v17, 0, v85, vcc
	v_cmp_gt_i32_e32 vcc, s8, v10
	v_readlane_b32 s8, v255, 18
	s_nop 0
	v_cndmask_b32_e32 v16, 0, v86, vcc
	v_cmp_gt_i32_e32 vcc, s8, v10
	v_readlane_b32 s8, v255, 19
	s_nop 0
	v_cndmask_b32_e32 v15, 0, v87, vcc
	v_cmp_gt_i32_e32 vcc, s8, v10
	s_nop 1
	v_cndmask_b32_e32 v14, 0, v88, vcc
	s_cbranch_scc1 .LBB0_759
	s_lshl_b32 s0, s0, 11
	s_add_i32 s0, s0, 0
	v_lshl_add_u32 v6, v10, 5, s0
	ds_read_b128 v[2:5], v6
	ds_read_b128 v[6:9], v6 offset:16
	s_mov_b32 s83, s78
	s_mov_b32 s77, s76
	s_mov_b32 s75, s74
	s_waitcnt lgkmcnt(1)
	v_add_u32_e32 v78, v2, v3
	v_add3_u32 v78, v78, v5, v4
	s_waitcnt lgkmcnt(0)
	v_add3_u32 v78, v78, v9, v8
	s_mov_b32 s73, s72
	s_mov_b32 s72, s70
	s_mov_b32 s76, s65
	s_mov_b32 s74, s63
	s_mov_b32 s69, s62
	s_mov_b32 s68, s58
	s_mov_b32 s66, s56
	s_mov_b32 s65, s55
	s_mov_b32 s64, s6
	s_mov_b32 s6, s51
	s_mov_b32 s58, s50
	s_mov_b64 s[62:63], s[48:49]
	s_mov_b32 s56, s43
	s_mov_b32 s49, s42
	s_mov_b32 s48, s41
	s_mov_b32 s91, s40
	s_mov_b32 s90, s39
	s_mov_b32 s89, s38
	s_mov_b32 s88, s2
	s_mov_b32 s2, s37
	s_mov_b32 s84, s7
	s_mov_b32 s7, s36
	s_mov_b32 s85, s35
	s_mov_b32 s44, s34
	s_mov_b32 s51, s31
	s_mov_b32 s50, s30
	s_mov_b32 s92, s29
	s_mov_b32 s71, s28
	s_mov_b32 s70, s27
	s_mov_b32 s81, s26
	s_mov_b32 s82, s25
	s_mov_b32 s55, s22
	v_add3_u32 v78, v78, v7, v6
	s_mov_b32 s9, 63
	s_nop 0
	v_readlane_b32 s25, v78, 63
	v_readlane_b32 s26, v78, 62
	v_readlane_b32 s27, v78, 61
	v_readlane_b32 s28, v78, 60
	v_readlane_b32 s29, v78, 59
	v_readlane_b32 s30, v78, 58
	v_readlane_b32 s31, v78, 57
	v_readlane_b32 s34, v78, 56
	v_readlane_b32 s35, v78, 55
	v_readlane_b32 s36, v78, 54
	v_readlane_b32 s37, v78, 53
	v_readlane_b32 s38, v78, 52
	v_readlane_b32 s39, v78, 51
	v_readlane_b32 s40, v78, 50
	v_readlane_b32 s41, v78, 49
	v_readlane_b32 s42, v78, 48
	s_mov_b32 s8, s1
	s_add_i32 s1, s8, s25
	s_cmpk_gt_u32 s1, 0xff
	s_cbranch_scc1 .Lthr_f63
	s_mov_b32 s8, s1
	s_add_i32 s1, s8, s26
	s_cmpk_gt_u32 s1, 0xff
	s_cbranch_scc1 .Lthr_f62
	s_mov_b32 s8, s1
	s_add_i32 s1, s8, s27
	s_cmpk_gt_u32 s1, 0xff
	s_cbranch_scc1 .Lthr_f61
	s_mov_b32 s8, s1
	s_add_i32 s1, s8, s28
	s_cmpk_gt_u32 s1, 0xff
	s_cbranch_scc1 .Lthr_f60
	s_mov_b32 s8, s1
	s_add_i32 s1, s8, s29
	s_cmpk_gt_u32 s1, 0xff
	s_cbranch_scc1 .Lthr_f59
	s_mov_b32 s8, s1
	s_add_i32 s1, s8, s30
	s_cmpk_gt_u32 s1, 0xff
	s_cbranch_scc1 .Lthr_f58
	s_mov_b32 s8, s1
	s_add_i32 s1, s8, s31
	s_cmpk_gt_u32 s1, 0xff
	s_cbranch_scc1 .Lthr_f57
	s_mov_b32 s8, s1
	s_add_i32 s1, s8, s34
	s_cmpk_gt_u32 s1, 0xff
	s_cbranch_scc1 .Lthr_f56
	s_mov_b32 s8, s1
	s_add_i32 s1, s8, s35
	s_cmpk_gt_u32 s1, 0xff
	s_cbranch_scc1 .Lthr_f55
	s_mov_b32 s8, s1
	s_add_i32 s1, s8, s36
	s_cmpk_gt_u32 s1, 0xff
	s_cbranch_scc1 .Lthr_f54
	s_mov_b32 s8, s1
	s_add_i32 s1, s8, s37
	s_cmpk_gt_u32 s1, 0xff
	s_cbranch_scc1 .Lthr_f53
	s_mov_b32 s8, s1
	s_add_i32 s1, s8, s38
	s_cmpk_gt_u32 s1, 0xff
	s_cbranch_scc1 .Lthr_f52
	s_mov_b32 s8, s1
	s_add_i32 s1, s8, s39
	s_cmpk_gt_u32 s1, 0xff
	s_cbranch_scc1 .Lthr_f51
	s_mov_b32 s8, s1
	s_add_i32 s1, s8, s40
	s_cmpk_gt_u32 s1, 0xff
	s_cbranch_scc1 .Lthr_f50
	s_mov_b32 s8, s1
	s_add_i32 s1, s8, s41
	s_cmpk_gt_u32 s1, 0xff
	s_cbranch_scc1 .Lthr_f49
	s_mov_b32 s8, s1
	s_add_i32 s1, s8, s42
	s_cmpk_gt_u32 s1, 0xff
	s_cbranch_scc1 .Lthr_f48
	s_mov_b32 s8, s1
	s_mov_b32 s9, 47
	s_branch .LBB0_723
.Lthr_f63:
	s_mov_b32 s0, 63
	s_branch .Lthr_found
.Lthr_f62:
	s_mov_b32 s0, 62
	s_branch .Lthr_found
.Lthr_f61:
	s_mov_b32 s0, 61
	s_branch .Lthr_found
.Lthr_f60:
	s_mov_b32 s0, 60
	s_branch .Lthr_found
.Lthr_f59:
	s_mov_b32 s0, 59
	s_branch .Lthr_found
.Lthr_f58:
	s_mov_b32 s0, 58
	s_branch .Lthr_found
.Lthr_f57:
	s_mov_b32 s0, 57
	s_branch .Lthr_found
.Lthr_f56:
	s_mov_b32 s0, 56
	s_branch .Lthr_found
.Lthr_f55:
	s_mov_b32 s0, 55
	s_branch .Lthr_found
.Lthr_f54:
	s_mov_b32 s0, 54
	s_branch .Lthr_found
.Lthr_f53:
	s_mov_b32 s0, 53
	s_branch .Lthr_found
.Lthr_f52:
	s_mov_b32 s0, 52
	s_branch .Lthr_found
.Lthr_f51:
	s_mov_b32 s0, 51
	s_branch .Lthr_found
.Lthr_f50:
	s_mov_b32 s0, 50
	s_branch .Lthr_found
.Lthr_f49:
	s_mov_b32 s0, 49
	s_branch .Lthr_found
.Lthr_f48:
	s_mov_b32 s0, 48
	s_branch .Lthr_found

.Lthr_found:
	v_readlane_b32 s1, v9, s0
	s_add_i32 s1, s1, s8
	s_cmpk_gt_u32 s1, 0xff
	s_cselect_b64 s[10:11], -1, 0
	s_and_b64 s[10:11], s[10:11], exec
	s_cselect_b32 s14, s8, s1
	v_readlane_b32 s8, v8, s0
	s_add_i32 s15, s14, s8
	s_cmpk_gt_u32 s15, 0xff
	s_cselect_b64 s[8:9], -1, 0
	s_and_b64 s[10:11], s[8:9], exec
	s_cselect_b32 s16, 6, 0
	s_cmpk_gt_u32 s1, 0xff
	s_cselect_b64 s[10:11], -1, 0
	s_and_b64 s[12:13], s[10:11], exec
	s_cselect_b32 s1, 7, s16
	s_or_b64 s[8:9], s[10:11], s[8:9]
	s_and_b64 s[10:11], s[8:9], exec
	s_cselect_b32 s14, s14, s15
	v_readlane_b32 s10, v7, s0
	s_add_i32 s15, s14, s10
	s_cmpk_gt_u32 s15, 0xff
	s_cselect_b64 s[10:11], -1, 0
	s_and_b64 s[12:13], s[10:11], exec
	s_cselect_b32 s16, 5, s1
	s_and_b64 s[12:13], s[8:9], exec
	s_cselect_b32 s1, s1, s16
	s_or_b64 s[8:9], s[8:9], s[10:11]
	s_and_b64 s[10:11], s[8:9], exec
	s_cselect_b32 s14, s14, s15
	v_readlane_b32 s10, v6, s0
	s_add_i32 s15, s14, s10
	s_cmpk_gt_u32 s15, 0xff
	s_cselect_b64 s[10:11], -1, 0
	s_and_b64 s[12:13], s[10:11], exec
	s_cselect_b32 s16, 4, s1
	s_and_b64 s[12:13], s[8:9], exec
	s_cselect_b32 s1, s1, s16
	s_or_b64 s[8:9], s[8:9], s[10:11]
	s_and_b64 s[10:11], s[8:9], exec
	s_cselect_b32 s14, s14, s15
	v_readlane_b32 s10, v5, s0
	s_add_i32 s15, s14, s10
	s_cmpk_gt_u32 s15, 0xff
	s_cselect_b64 s[10:11], -1, 0
	s_and_b64 s[12:13], s[10:11], exec
	s_cselect_b32 s16, 3, s1
	s_and_b64 s[12:13], s[8:9], exec
	s_cselect_b32 s1, s1, s16
	s_or_b64 s[8:9], s[8:9], s[10:11]
	s_and_b64 s[10:11], s[8:9], exec
	s_cselect_b32 s14, s14, s15
	v_readlane_b32 s10, v4, s0
	s_add_i32 s15, s14, s10
	s_cmpk_gt_u32 s15, 0xff
	s_cselect_b64 s[10:11], -1, 0
	s_and_b64 s[12:13], s[10:11], exec
	s_cselect_b32 s16, 2, s1
	s_and_b64 s[12:13], s[8:9], exec
	s_cselect_b32 s1, s1, s16
	s_or_b64 s[8:9], s[8:9], s[10:11]
	s_and_b64 s[10:11], s[8:9], exec
	s_cselect_b32 s14, s14, s15
	v_readlane_b32 s10, v3, s0
	s_add_i32 s15, s14, s10
	s_cmpk_gt_u32 s15, 0xff
	s_cselect_b64 s[10:11], -1, 0
	s_and_b64 s[12:13], s[10:11], exec
	s_cselect_b32 s16, 1, s1
	s_and_b64 s[12:13], s[8:9], exec
	s_cselect_b32 s1, s1, s16
	s_or_b64 s[8:9], s[8:9], s[10:11]
	s_and_b64 s[10:11], s[8:9], exec
	s_cselect_b32 s10, s14, s15
	v_readlane_b32 s11, v2, s0
	s_add_i32 s10, s10, s11
	s_cmpk_lt_u32 s10, 0x100
	s_cselect_b64 s[10:11], -1, 0
	s_or_b64 s[8:9], s[8:9], s[10:11]
	s_and_b64 s[8:9], s[8:9], exec
	s_cselect_b32 s94, s1, 0
	s_lshl_b32 s0, s0, 3
	s_add_i32 s94, s94, s0
	v_readlane_b32 s0, v254, 54
	s_lshl_b32 s22, s94, 7
	v_mov_b32_e32 v91, 0
	v_mov_b32_e32 v7, 0xffff0000
	v_lshl_add_u32 v79, v10, 2, s0
	s_and_b64 vcc, exec, s[60:61]
	s_cbranch_vccz .LBB0_726
	v_cmp_ge_u32_sdwa vcc, v77, s22 src0_sel:WORD_0 src1_sel:DWORD
	s_mov_b32 s0, 0xffff
	v_lshl_or_b32 v2, v77, 16, s0
	v_lshl_add_u32 v5, v91, 8, v79
	ds_write_b32 v5, v2
	v_addc_co_u32_e32 v91, vcc, 0, v91, vcc
	v_cmp_ge_u32_sdwa vcc, v77, s22 src0_sel:WORD_1 src1_sel:DWORD
	s_mov_b32 s1, 0xfffe
	v_and_or_b32 v3, v77, v7, s1
	v_lshl_add_u32 v6, v91, 8, v79
	ds_write_b32 v6, v3
	v_addc_co_u32_e32 v91, vcc, 0, v91, vcc
	v_cmp_ge_u32_sdwa vcc, v76, s22 src0_sel:WORD_0 src1_sel:DWORD
	s_mov_b32 s0, 0xff7f
	v_lshl_or_b32 v4, v76, 16, s0
	v_lshl_add_u32 v5, v91, 8, v79
	ds_write_b32 v5, v4
	v_addc_co_u32_e32 v91, vcc, 0, v91, vcc
	v_cmp_ge_u32_sdwa vcc, v76, s22 src0_sel:WORD_1 src1_sel:DWORD
	s_mov_b32 s1, 0xff7e
	v_and_or_b32 v2, v76, v7, s1
	v_lshl_add_u32 v6, v91, 8, v79
	ds_write_b32 v6, v2
	v_addc_co_u32_e32 v91, vcc, 0, v91, vcc
	v_cmp_ge_u32_sdwa vcc, v75, s22 src0_sel:WORD_0 src1_sel:DWORD
	s_mov_b32 s0, 0xfeff
	v_lshl_or_b32 v3, v75, 16, s0
	v_lshl_add_u32 v5, v91, 8, v79
	ds_write_b32 v5, v3
	v_addc_co_u32_e32 v91, vcc, 0, v91, vcc
	v_cmp_ge_u32_sdwa vcc, v75, s22 src0_sel:WORD_1 src1_sel:DWORD
	s_mov_b32 s1, 0xfefe
	v_and_or_b32 v4, v75, v7, s1
	v_lshl_add_u32 v6, v91, 8, v79
	ds_write_b32 v6, v4
	v_addc_co_u32_e32 v91, vcc, 0, v91, vcc
	v_cmp_ge_u32_sdwa vcc, v74, s22 src0_sel:WORD_0 src1_sel:DWORD
	s_mov_b32 s0, 0xfe7f
	v_lshl_or_b32 v2, v74, 16, s0
	v_lshl_add_u32 v5, v91, 8, v79
	ds_write_b32 v5, v2
	v_addc_co_u32_e32 v91, vcc, 0, v91, vcc
	v_cmp_ge_u32_sdwa vcc, v74, s22 src0_sel:WORD_1 src1_sel:DWORD
	s_mov_b32 s1, 0xfe7e
	v_and_or_b32 v3, v74, v7, s1
	v_lshl_add_u32 v6, v91, 8, v79
	ds_write_b32 v6, v3
	v_addc_co_u32_e32 v91, vcc, 0, v91, vcc
	v_min_u32_e32 v91, 21, v91
	v_cmp_ge_u32_sdwa vcc, v73, s22 src0_sel:WORD_0 src1_sel:DWORD
	s_mov_b32 s0, 0xfdff
	v_lshl_or_b32 v4, v73, 16, s0
	v_lshl_add_u32 v5, v91, 8, v79
	ds_write_b32 v5, v4
	v_addc_co_u32_e32 v91, vcc, 0, v91, vcc
	v_cmp_ge_u32_sdwa vcc, v73, s22 src0_sel:WORD_1 src1_sel:DWORD
	s_mov_b32 s1, 0xfdfe
	v_and_or_b32 v2, v73, v7, s1
	v_lshl_add_u32 v6, v91, 8, v79
	ds_write_b32 v6, v2
	v_addc_co_u32_e32 v91, vcc, 0, v91, vcc
	v_cmp_ge_u32_sdwa vcc, v72, s22 src0_sel:WORD_0 src1_sel:DWORD
	s_mov_b32 s0, 0xfd7f
	v_lshl_or_b32 v3, v72, 16, s0
	v_lshl_add_u32 v5, v91, 8, v79
	ds_write_b32 v5, v3
	v_addc_co_u32_e32 v91, vcc, 0, v91, vcc
	v_cmp_ge_u32_sdwa vcc, v72, s22 src0_sel:WORD_1 src1_sel:DWORD
	s_mov_b32 s1, 0xfd7e
	v_and_or_b32 v4, v72, v7, s1
	v_lshl_add_u32 v6, v91, 8, v79
	ds_write_b32 v6, v4
	v_addc_co_u32_e32 v91, vcc, 0, v91, vcc
	v_cmp_ge_u32_sdwa vcc, v71, s22 src0_sel:WORD_0 src1_sel:DWORD
	s_mov_b32 s0, 0xfcff
	v_lshl_or_b32 v2, v71, 16, s0
	v_lshl_add_u32 v5, v91, 8, v79
	ds_write_b32 v5, v2
	v_addc_co_u32_e32 v91, vcc, 0, v91, vcc
	v_cmp_ge_u32_sdwa vcc, v71, s22 src0_sel:WORD_1 src1_sel:DWORD
	s_mov_b32 s1, 0xfcfe
	v_and_or_b32 v3, v71, v7, s1
	v_lshl_add_u32 v6, v91, 8, v79
	ds_write_b32 v6, v3
	v_addc_co_u32_e32 v91, vcc, 0, v91, vcc
	v_cmp_ge_u32_sdwa vcc, v70, s22 src0_sel:WORD_0 src1_sel:DWORD
	s_mov_b32 s0, 0xfc7f
	v_lshl_or_b32 v4, v70, 16, s0
	v_lshl_add_u32 v5, v91, 8, v79
	ds_write_b32 v5, v4
	v_addc_co_u32_e32 v91, vcc, 0, v91, vcc
	v_cmp_ge_u32_sdwa vcc, v70, s22 src0_sel:WORD_1 src1_sel:DWORD
	s_mov_b32 s1, 0xfc7e
	v_and_or_b32 v2, v70, v7, s1
	v_lshl_add_u32 v6, v91, 8, v79
	ds_write_b32 v6, v2
	v_addc_co_u32_e32 v91, vcc, 0, v91, vcc
	v_min_u32_e32 v91, 21, v91
